# P0 pool-fold items dealt to the even waves of all workgroups (was all waves of half the workgroups); plus P2 pipeline and epilogue load hoists
# speedup vs baseline: 1.0029x; 1.0029x over previous
.LBB0_100:
	v_readlane_b32 s44, v242, 8
	s_bitcmp1_b32 s0, 0
	v_readlane_b32 s45, v242, 9
	s_cbranch_scc1 .LBB0_105
	s_waitcnt vmcnt(15)
	v_lshlrev_b32_e32 v2, 4, v0
	s_waitcnt vmcnt(12)
	v_and_b32_e32 v14, 0x1f0, v2
	v_or_b32_e32 v2, 64, v146
	s_waitcnt vmcnt(4)
	v_lshrrev_b32_e32 v54, 5, v2
	v_or_b32_e32 v2, 0x80, v146
	v_lshrrev_b32_e32 v55, 5, v2
	v_or_b32_e32 v2, 0xc0, v146
	v_lshrrev_b32_e32 v56, 5, v2
	v_or_b32_e32 v2, 0x100, v146
	v_lshrrev_b32_e32 v57, 5, v2
	v_or_b32_e32 v2, 0x140, v146
	v_lshrrev_b32_e32 v58, 5, v2
	v_or_b32_e32 v2, 0x180, v146
	v_readlane_b32 s10, v242, 6
	v_mov_b32_e32 v15, 0
	v_lshrrev_b32_e32 v59, 5, v2
	v_or_b32_e32 v2, 0x1c0, v146
	s_lshl_b32 s4, s94, 6
	v_readlane_b32 s11, v242, 7
	s_lshl_b32 s5, s10, 3
	v_lshl_add_u64 v[16:17], s[56:57], 0, v[14:15]
	v_lshl_add_u64 v[18:19], s[58:59], 0, v[14:15]
	v_lshrrev_b32_e32 v52, 5, v146
	v_lshl_add_u32 v53, v146, 4, s3
	v_lshrrev_b32_e32 v60, 5, v2
	s_add_i32 s9, s4, s5
	s_lshr_b32 s9, s9, 1
	s_lshl_b32 s18, s88, 6
	s_mov_b64 s[4:5], 0xc00000
	s_movk_i32 s19, 0x2000
	s_mov_b32 s11, 0
	s_movk_i32 s20, 0x4000
	s_movk_i32 s21, 0x6000
	s_mov_b32 s22, 0x8000
	s_mov_b32 s23, 0xa000
	s_mov_b32 s24, 0xc000
	s_mov_b32 s25, 0xe000
	s_mov_b32 s26, 0x10000
	s_mov_b32 s27, 0x12000
	s_mov_b32 s28, 0x14000
	s_mov_b32 s29, 0x16000
	s_mov_b32 s30, 0x18000
	s_mov_b32 s31, 0x1a000
	s_mov_b32 s33, 0x1c000
	s_mov_b32 s34, 0x1e000
	s_mov_b64 s[12:13], 0x1c00c00
	s_lshr_b32 s35, s0, 1
